# RG-LRU scan rewrite with the v_readlane->VALU SGPR wait-state distance fixed (2 states); otherwise identical
# baseline (speedup 1.0000x reference)
.LBB0_460:
	s_or_b64 exec, exec, s[0:1]
	v_readlane_b32 s0, v255, 33
	s_waitcnt lgkmcnt(0)
	s_barrier
	v_mov_b32_e32 v0, s0
	ds_read_b32 v0, v0
	s_movk_i32 s0, 0x10f
	s_waitcnt lgkmcnt(0)
	s_barrier
	v_cmp_lt_i32_e32 vcc, s0, v0
	v_readfirstlane_b32 s22, v0
	s_mov_b64 s[0:1], -1
	s_cbranch_vccnz .LBB0_455
	s_cmp_gt_i32 s22, 15
	s_cbranch_scc0 .LBB0_745
	v_readlane_b32 s13, v254, 27
	s_add_i32 s0, s22, -16
	s_lshr_b32 s1, s0, 6
	s_and_b32 s0, s0, 63
	s_lshl_b32 s23, s0, 3
	s_lshl_b32 s26, s1, 12
	s_lshl_b32 s27, s1, 8
	s_or_b32 s27, s27, 0x4000
	v_mbcnt_lo_u32_b32 v0, -1, 0
	v_mbcnt_hi_u32_b32 v0, -1, v0
	v_mov_b32_e32 v1, v0
	v_add_u32_e32 v0, s13, v0
	s_lshr_b32 s12, s13, 6
	v_and_b32_e32 v2, 1, v0
	v_lshrrev_b32_e32 v4, 1, v0
	v_mul_u32_u24_e32 v4, 17, v4
	v_lshl_add_u32 v5, v2, 2, s23
	v_lshlrev_b32_e32 v5, 2, v5
	v_lshlrev_b32_e32 v7, 2, v1
	v_sub_u32_e32 v6, 0x100, v4
	v_max_i32_e32 v6, 0, v6
	v_lshlrev_b32_e32 v8, 5, v2
	v_lshrrev_b32_e32 v15, 1, v5
	v_sub_u32_e32 v15, 0x400, v15
	s_movk_i32 s14, 0x1400
	s_add_u32 s8, s18, 0x2200000
	s_addc_u32 s9, s19, 0
	s_add_u32 s10, s20, 0x1100000
	s_addc_u32 s11, s21, 0
	s_addk_i32 s27, 0xff
	s_add_i32 s13, s26, 0x10ff
	v_sub_u32_e32 v9, s27, v4
	v_sub_u32_e32 v10, s13, v4
	s_addk_i32 s27, 0xff01
	v_lshl_add_u32 v11, v9, 11, v5
	v_lshl_add_u32 v12, v10, 11, v5
	v_cmp_lt_u32_e32 vcc, 0, v6
	v_cmp_lt_u32_e64 s[36:37], 1, v6
	s_nop 0
	v_cndmask_b32_e32 v248, v12, v11, vcc
	v_cndmask_b32_e64 v249, v12, v11, s[36:37]
	v_add_u32_e32 v249, 0xfffff800, v249
	global_load_dwordx4 v[16:19], v248, s[8:9]
	v_lshrrev_b32_e32 v250, 1, v248
	global_load_dwordx2 v[84:85], v250, s[10:11]
	global_load_dwordx4 v[20:23], v249, s[8:9]
	v_lshrrev_b32_e32 v250, 1, v249
	global_load_dwordx2 v[86:87], v250, s[10:11]
	v_cmp_lt_u32_e32 vcc, 2, v6
	v_cmp_lt_u32_e64 s[36:37], 3, v6
	s_nop 0
	v_cndmask_b32_e32 v248, v12, v11, vcc
	v_cndmask_b32_e64 v249, v12, v11, s[36:37]
	v_add_u32_e32 v248, 0xfffff000, v248
	v_add_u32_e32 v249, 0xffffe800, v249
	global_load_dwordx4 v[24:27], v248, s[8:9]
	v_lshrrev_b32_e32 v250, 1, v248
	global_load_dwordx2 v[88:89], v250, s[10:11]
	global_load_dwordx4 v[28:31], v249, s[8:9]
	v_lshrrev_b32_e32 v250, 1, v249
	global_load_dwordx2 v[90:91], v250, s[10:11]
	v_cmp_lt_u32_e32 vcc, 4, v6
	v_cmp_lt_u32_e64 s[36:37], 5, v6
	s_nop 0
	v_cndmask_b32_e32 v248, v12, v11, vcc
	v_cndmask_b32_e64 v249, v12, v11, s[36:37]
	v_add_u32_e32 v248, 0xffffe000, v248
	v_add_u32_e32 v249, 0xffffd800, v249
	global_load_dwordx4 v[32:35], v248, s[8:9]
	v_lshrrev_b32_e32 v250, 1, v248
	global_load_dwordx2 v[92:93], v250, s[10:11]
	global_load_dwordx4 v[36:39], v249, s[8:9]
	v_lshrrev_b32_e32 v250, 1, v249
	global_load_dwordx2 v[94:95], v250, s[10:11]
	v_cmp_lt_u32_e32 vcc, 6, v6
	v_cmp_lt_u32_e64 s[36:37], 7, v6
	s_nop 0
	v_cndmask_b32_e32 v248, v12, v11, vcc
	v_cndmask_b32_e64 v249, v12, v11, s[36:37]
	v_add_u32_e32 v248, 0xffffd000, v248
	v_add_u32_e32 v249, 0xffffc800, v249
	global_load_dwordx4 v[40:43], v248, s[8:9]
	v_lshrrev_b32_e32 v250, 1, v248
	global_load_dwordx2 v[96:97], v250, s[10:11]
	global_load_dwordx4 v[44:47], v249, s[8:9]
	v_lshrrev_b32_e32 v250, 1, v249
	global_load_dwordx2 v[98:99], v250, s[10:11]
	v_cmp_lt_u32_e32 vcc, 8, v6
	v_cmp_lt_u32_e64 s[36:37], 9, v6
	s_nop 0
	v_cndmask_b32_e32 v248, v12, v11, vcc
	v_cndmask_b32_e64 v249, v12, v11, s[36:37]
	v_add_u32_e32 v248, 0xffffc000, v248
	v_add_u32_e32 v249, 0xffffb800, v249
	global_load_dwordx4 v[48:51], v248, s[8:9]
	v_lshrrev_b32_e32 v250, 1, v248
	global_load_dwordx2 v[100:101], v250, s[10:11]
	global_load_dwordx4 v[52:55], v249, s[8:9]
	v_lshrrev_b32_e32 v250, 1, v249
	global_load_dwordx2 v[102:103], v250, s[10:11]
	v_cmp_lt_u32_e32 vcc, 10, v6
	v_cmp_lt_u32_e64 s[36:37], 11, v6
	s_nop 0
	v_cndmask_b32_e32 v248, v12, v11, vcc
	v_cndmask_b32_e64 v249, v12, v11, s[36:37]
	v_add_u32_e32 v248, 0xffffb000, v248
	v_add_u32_e32 v249, 0xffffa800, v249
	global_load_dwordx4 v[56:59], v248, s[8:9]
	v_lshrrev_b32_e32 v250, 1, v248
	global_load_dwordx2 v[104:105], v250, s[10:11]
	global_load_dwordx4 v[60:63], v249, s[8:9]
	v_lshrrev_b32_e32 v250, 1, v249
	global_load_dwordx2 v[106:107], v250, s[10:11]
	v_cmp_lt_u32_e32 vcc, 12, v6
	v_cmp_lt_u32_e64 s[36:37], 13, v6
	s_nop 0
	v_cndmask_b32_e32 v248, v12, v11, vcc
	v_cndmask_b32_e64 v249, v12, v11, s[36:37]
	v_add_u32_e32 v248, 0xffffa000, v248
	v_add_u32_e32 v249, 0xffff9800, v249
	global_load_dwordx4 v[64:67], v248, s[8:9]
	v_lshrrev_b32_e32 v250, 1, v248
	global_load_dwordx2 v[108:109], v250, s[10:11]
	global_load_dwordx4 v[68:71], v249, s[8:9]
	v_lshrrev_b32_e32 v250, 1, v249
	global_load_dwordx2 v[110:111], v250, s[10:11]
	v_cmp_lt_u32_e32 vcc, 14, v6
	v_cmp_lt_u32_e64 s[36:37], 15, v6
	s_nop 0
	v_cndmask_b32_e32 v248, v12, v11, vcc
	v_cndmask_b32_e64 v249, v12, v11, s[36:37]
	v_add_u32_e32 v248, 0xffff9000, v248
	v_add_u32_e32 v249, 0xffff8800, v249
	global_load_dwordx4 v[72:75], v248, s[8:9]
	v_lshrrev_b32_e32 v250, 1, v248
	global_load_dwordx2 v[112:113], v250, s[10:11]
	global_load_dwordx4 v[76:79], v249, s[8:9]
	v_lshrrev_b32_e32 v250, 1, v249
	global_load_dwordx2 v[114:115], v250, s[10:11]
	v_cmp_lt_u32_e32 vcc, 16, v6
	s_nop 1
	v_cndmask_b32_e32 v248, v12, v11, vcc
	v_add_u32_e32 v248, 0xffff8000, v248
	global_load_dwordx4 v[80:83], v248, s[8:9]
	v_lshrrev_b32_e32 v250, 1, v248
	global_load_dwordx2 v[116:117], v250, s[10:11]
	s_waitcnt vmcnt(32)
	v_lshlrev_b32_e32 v224, 16, v84
	v_and_b32_e32 v225, 0xffff0000, v84
	v_lshlrev_b32_e32 v226, 16, v85
	v_and_b32_e32 v227, 0xffff0000, v85
	v_mov_b32_e32 v220, v16
	v_mov_b32_e32 v221, v17
	v_mov_b32_e32 v222, v18
	v_mov_b32_e32 v223, v19
	s_waitcnt vmcnt(30)
	v_lshlrev_b32_e32 v248, 16, v86
	v_and_b32_e32 v249, 0xffff0000, v86
	v_lshlrev_b32_e32 v250, 16, v87
	v_and_b32_e32 v251, 0xffff0000, v87
	v_fma_f32 v224, v20, v224, v248
	v_fma_f32 v225, v21, v225, v249
	v_fma_f32 v226, v22, v226, v250
	v_fma_f32 v227, v23, v227, v251
	v_mul_f32_e32 v220, v220, v20
	v_mul_f32_e32 v221, v221, v21
	v_mul_f32_e32 v222, v222, v22
	v_mul_f32_e32 v223, v223, v23
	s_waitcnt vmcnt(28)
	v_lshlrev_b32_e32 v248, 16, v88
	v_and_b32_e32 v249, 0xffff0000, v88
	v_lshlrev_b32_e32 v250, 16, v89
	v_and_b32_e32 v251, 0xffff0000, v89
	v_fma_f32 v224, v24, v224, v248
	v_fma_f32 v225, v25, v225, v249
	v_fma_f32 v226, v26, v226, v250
	v_fma_f32 v227, v27, v227, v251
	v_mul_f32_e32 v220, v220, v24
	v_mul_f32_e32 v221, v221, v25
	v_mul_f32_e32 v222, v222, v26
	v_mul_f32_e32 v223, v223, v27
	s_waitcnt vmcnt(26)
	v_lshlrev_b32_e32 v248, 16, v90
	v_and_b32_e32 v249, 0xffff0000, v90
	v_lshlrev_b32_e32 v250, 16, v91
	v_and_b32_e32 v251, 0xffff0000, v91
	v_fma_f32 v224, v28, v224, v248
	v_fma_f32 v225, v29, v225, v249
	v_fma_f32 v226, v30, v226, v250
	v_fma_f32 v227, v31, v227, v251
	v_mul_f32_e32 v220, v220, v28
	v_mul_f32_e32 v221, v221, v29
	v_mul_f32_e32 v222, v222, v30
	v_mul_f32_e32 v223, v223, v31
	s_waitcnt vmcnt(24)
	v_lshlrev_b32_e32 v248, 16, v92
	v_and_b32_e32 v249, 0xffff0000, v92
	v_lshlrev_b32_e32 v250, 16, v93
	v_and_b32_e32 v251, 0xffff0000, v93
	v_fma_f32 v224, v32, v224, v248
	v_fma_f32 v225, v33, v225, v249
	v_fma_f32 v226, v34, v226, v250
	v_fma_f32 v227, v35, v227, v251
	v_mul_f32_e32 v220, v220, v32
	v_mul_f32_e32 v221, v221, v33
	v_mul_f32_e32 v222, v222, v34
	v_mul_f32_e32 v223, v223, v35
	s_waitcnt vmcnt(22)
	v_lshlrev_b32_e32 v248, 16, v94
	v_and_b32_e32 v249, 0xffff0000, v94
	v_lshlrev_b32_e32 v250, 16, v95
	v_and_b32_e32 v251, 0xffff0000, v95
	v_fma_f32 v224, v36, v224, v248
	v_fma_f32 v225, v37, v225, v249
	v_fma_f32 v226, v38, v226, v250
	v_fma_f32 v227, v39, v227, v251
	v_mul_f32_e32 v220, v220, v36
	v_mul_f32_e32 v221, v221, v37
	v_mul_f32_e32 v222, v222, v38
	v_mul_f32_e32 v223, v223, v39
	s_waitcnt vmcnt(20)
	v_lshlrev_b32_e32 v248, 16, v96
	v_and_b32_e32 v249, 0xffff0000, v96
	v_lshlrev_b32_e32 v250, 16, v97
	v_and_b32_e32 v251, 0xffff0000, v97
	v_fma_f32 v224, v40, v224, v248
	v_fma_f32 v225, v41, v225, v249
	v_fma_f32 v226, v42, v226, v250
	v_fma_f32 v227, v43, v227, v251
	v_mul_f32_e32 v220, v220, v40
	v_mul_f32_e32 v221, v221, v41
	v_mul_f32_e32 v222, v222, v42
	v_mul_f32_e32 v223, v223, v43
	s_waitcnt vmcnt(18)
	v_lshlrev_b32_e32 v248, 16, v98
	v_and_b32_e32 v249, 0xffff0000, v98
	v_lshlrev_b32_e32 v250, 16, v99
	v_and_b32_e32 v251, 0xffff0000, v99
	v_fma_f32 v224, v44, v224, v248
	v_fma_f32 v225, v45, v225, v249
	v_fma_f32 v226, v46, v226, v250
	v_fma_f32 v227, v47, v227, v251
	v_mul_f32_e32 v220, v220, v44
	v_mul_f32_e32 v221, v221, v45
	v_mul_f32_e32 v222, v222, v46
	v_mul_f32_e32 v223, v223, v47
	s_waitcnt vmcnt(16)
	v_lshlrev_b32_e32 v248, 16, v100
	v_and_b32_e32 v249, 0xffff0000, v100
	v_lshlrev_b32_e32 v250, 16, v101
	v_and_b32_e32 v251, 0xffff0000, v101
	v_fma_f32 v224, v48, v224, v248
	v_fma_f32 v225, v49, v225, v249
	v_fma_f32 v226, v50, v226, v250
	v_fma_f32 v227, v51, v227, v251
	v_mul_f32_e32 v220, v220, v48
	v_mul_f32_e32 v221, v221, v49
	v_mul_f32_e32 v222, v222, v50
	v_mul_f32_e32 v223, v223, v51
	s_waitcnt vmcnt(14)
	v_lshlrev_b32_e32 v248, 16, v102
	v_and_b32_e32 v249, 0xffff0000, v102
	v_lshlrev_b32_e32 v250, 16, v103
	v_and_b32_e32 v251, 0xffff0000, v103
	v_fma_f32 v224, v52, v224, v248
	v_fma_f32 v225, v53, v225, v249
	v_fma_f32 v226, v54, v226, v250
	v_fma_f32 v227, v55, v227, v251
	v_mul_f32_e32 v220, v220, v52
	v_mul_f32_e32 v221, v221, v53
	v_mul_f32_e32 v222, v222, v54
	v_mul_f32_e32 v223, v223, v55
	s_waitcnt vmcnt(12)
	v_lshlrev_b32_e32 v248, 16, v104
	v_and_b32_e32 v249, 0xffff0000, v104
	v_lshlrev_b32_e32 v250, 16, v105
	v_and_b32_e32 v251, 0xffff0000, v105
	v_fma_f32 v224, v56, v224, v248
	v_fma_f32 v225, v57, v225, v249
	v_fma_f32 v226, v58, v226, v250
	v_fma_f32 v227, v59, v227, v251
	v_mul_f32_e32 v220, v220, v56
	v_mul_f32_e32 v221, v221, v57
	v_mul_f32_e32 v222, v222, v58
	v_mul_f32_e32 v223, v223, v59
	s_waitcnt vmcnt(10)
	v_lshlrev_b32_e32 v248, 16, v106
	v_and_b32_e32 v249, 0xffff0000, v106
	v_lshlrev_b32_e32 v250, 16, v107
	v_and_b32_e32 v251, 0xffff0000, v107
	v_fma_f32 v224, v60, v224, v248
	v_fma_f32 v225, v61, v225, v249
	v_fma_f32 v226, v62, v226, v250
	v_fma_f32 v227, v63, v227, v251
	v_mul_f32_e32 v220, v220, v60
	v_mul_f32_e32 v221, v221, v61
	v_mul_f32_e32 v222, v222, v62
	v_mul_f32_e32 v223, v223, v63
	s_waitcnt vmcnt(8)
	v_lshlrev_b32_e32 v248, 16, v108
	v_and_b32_e32 v249, 0xffff0000, v108
	v_lshlrev_b32_e32 v250, 16, v109
	v_and_b32_e32 v251, 0xffff0000, v109
	v_fma_f32 v224, v64, v224, v248
	v_fma_f32 v225, v65, v225, v249
	v_fma_f32 v226, v66, v226, v250
	v_fma_f32 v227, v67, v227, v251
	v_mul_f32_e32 v220, v220, v64
	v_mul_f32_e32 v221, v221, v65
	v_mul_f32_e32 v222, v222, v66
	v_mul_f32_e32 v223, v223, v67
	s_waitcnt vmcnt(6)
	v_lshlrev_b32_e32 v248, 16, v110
	v_and_b32_e32 v249, 0xffff0000, v110
	v_lshlrev_b32_e32 v250, 16, v111
	v_and_b32_e32 v251, 0xffff0000, v111
	v_fma_f32 v224, v68, v224, v248
	v_fma_f32 v225, v69, v225, v249
	v_fma_f32 v226, v70, v226, v250
	v_fma_f32 v227, v71, v227, v251
	v_mul_f32_e32 v220, v220, v68
	v_mul_f32_e32 v221, v221, v69
	v_mul_f32_e32 v222, v222, v70
	v_mul_f32_e32 v223, v223, v71
	s_waitcnt vmcnt(4)
	v_lshlrev_b32_e32 v248, 16, v112
	v_and_b32_e32 v249, 0xffff0000, v112
	v_lshlrev_b32_e32 v250, 16, v113
	v_and_b32_e32 v251, 0xffff0000, v113
	v_fma_f32 v224, v72, v224, v248
	v_fma_f32 v225, v73, v225, v249
	v_fma_f32 v226, v74, v226, v250
	v_fma_f32 v227, v75, v227, v251
	v_mul_f32_e32 v220, v220, v72
	v_mul_f32_e32 v221, v221, v73
	v_mul_f32_e32 v222, v222, v74
	v_mul_f32_e32 v223, v223, v75
	s_waitcnt vmcnt(2)
	v_lshlrev_b32_e32 v248, 16, v114
	v_and_b32_e32 v249, 0xffff0000, v114
	v_lshlrev_b32_e32 v250, 16, v115
	v_and_b32_e32 v251, 0xffff0000, v115
	v_fma_f32 v224, v76, v224, v248
	v_fma_f32 v225, v77, v225, v249
	v_fma_f32 v226, v78, v226, v250
	v_fma_f32 v227, v79, v227, v251
	v_mul_f32_e32 v220, v220, v76
	v_mul_f32_e32 v221, v221, v77
	v_mul_f32_e32 v222, v222, v78
	v_mul_f32_e32 v223, v223, v79
	s_waitcnt vmcnt(0)
	v_lshlrev_b32_e32 v248, 16, v116
	v_and_b32_e32 v249, 0xffff0000, v116
	v_lshlrev_b32_e32 v250, 16, v117
	v_and_b32_e32 v251, 0xffff0000, v117
	v_fma_f32 v224, v80, v224, v248
	v_fma_f32 v225, v81, v225, v249
	v_fma_f32 v226, v82, v226, v250
	v_fma_f32 v227, v83, v227, v251
	v_mul_f32_e32 v220, v220, v80
	v_mul_f32_e32 v221, v221, v81
	v_mul_f32_e32 v222, v222, v82
	v_mul_f32_e32 v223, v223, v83
	v_cmp_le_u32_e32 vcc, 2, v1
	v_add_u32_e32 v252, 0xfffffff8, v7
	ds_bpermute_b32 v228, v252, v220
	ds_bpermute_b32 v229, v252, v221
	ds_bpermute_b32 v230, v252, v222
	ds_bpermute_b32 v231, v252, v223
	ds_bpermute_b32 v232, v252, v224
	ds_bpermute_b32 v233, v252, v225
	ds_bpermute_b32 v234, v252, v226
	ds_bpermute_b32 v235, v252, v227
	s_waitcnt lgkmcnt(0)
	v_fma_f32 v248, v220, v232, v224
	v_fma_f32 v249, v221, v233, v225
	v_fma_f32 v250, v222, v234, v226
	v_fma_f32 v251, v223, v235, v227
	v_mul_f32_e32 v228, v220, v228
	v_mul_f32_e32 v229, v221, v229
	v_mul_f32_e32 v230, v222, v230
	v_mul_f32_e32 v231, v223, v231
	v_cndmask_b32_e32 v224, v224, v248, vcc
	v_cndmask_b32_e32 v225, v225, v249, vcc
	v_cndmask_b32_e32 v226, v226, v250, vcc
	v_cndmask_b32_e32 v227, v227, v251, vcc
	v_cndmask_b32_e32 v220, v220, v228, vcc
	v_cndmask_b32_e32 v221, v221, v229, vcc
	v_cndmask_b32_e32 v222, v222, v230, vcc
	v_cndmask_b32_e32 v223, v223, v231, vcc
	v_cmp_le_u32_e32 vcc, 4, v1
	v_add_u32_e32 v252, 0xfffffff0, v7
	ds_bpermute_b32 v228, v252, v220
	ds_bpermute_b32 v229, v252, v221
	ds_bpermute_b32 v230, v252, v222
	ds_bpermute_b32 v231, v252, v223
	ds_bpermute_b32 v232, v252, v224
	ds_bpermute_b32 v233, v252, v225
	ds_bpermute_b32 v234, v252, v226
	ds_bpermute_b32 v235, v252, v227
	s_waitcnt lgkmcnt(0)
	v_fma_f32 v248, v220, v232, v224
	v_fma_f32 v249, v221, v233, v225
	v_fma_f32 v250, v222, v234, v226
	v_fma_f32 v251, v223, v235, v227
	v_mul_f32_e32 v228, v220, v228
	v_mul_f32_e32 v229, v221, v229
	v_mul_f32_e32 v230, v222, v230
	v_mul_f32_e32 v231, v223, v231
	v_cndmask_b32_e32 v224, v224, v248, vcc
	v_cndmask_b32_e32 v225, v225, v249, vcc
	v_cndmask_b32_e32 v226, v226, v250, vcc
	v_cndmask_b32_e32 v227, v227, v251, vcc
	v_cndmask_b32_e32 v220, v220, v228, vcc
	v_cndmask_b32_e32 v221, v221, v229, vcc
	v_cndmask_b32_e32 v222, v222, v230, vcc
	v_cndmask_b32_e32 v223, v223, v231, vcc
	v_cmp_le_u32_e32 vcc, 8, v1
	v_add_u32_e32 v252, 0xffffffe0, v7
	ds_bpermute_b32 v228, v252, v220
	ds_bpermute_b32 v229, v252, v221
	ds_bpermute_b32 v230, v252, v222
	ds_bpermute_b32 v231, v252, v223
	ds_bpermute_b32 v232, v252, v224
	ds_bpermute_b32 v233, v252, v225
	ds_bpermute_b32 v234, v252, v226
	ds_bpermute_b32 v235, v252, v227
	s_waitcnt lgkmcnt(0)
	v_fma_f32 v248, v220, v232, v224
	v_fma_f32 v249, v221, v233, v225
	v_fma_f32 v250, v222, v234, v226
	v_fma_f32 v251, v223, v235, v227
	v_mul_f32_e32 v228, v220, v228
	v_mul_f32_e32 v229, v221, v229
	v_mul_f32_e32 v230, v222, v230
	v_mul_f32_e32 v231, v223, v231
	v_cndmask_b32_e32 v224, v224, v248, vcc
	v_cndmask_b32_e32 v225, v225, v249, vcc
	v_cndmask_b32_e32 v226, v226, v250, vcc
	v_cndmask_b32_e32 v227, v227, v251, vcc
	v_cndmask_b32_e32 v220, v220, v228, vcc
	v_cndmask_b32_e32 v221, v221, v229, vcc
	v_cndmask_b32_e32 v222, v222, v230, vcc
	v_cndmask_b32_e32 v223, v223, v231, vcc
	v_cmp_le_u32_e32 vcc, 16, v1
	v_add_u32_e32 v252, 0xffffffc0, v7
	ds_bpermute_b32 v228, v252, v220
	ds_bpermute_b32 v229, v252, v221
	ds_bpermute_b32 v230, v252, v222
	ds_bpermute_b32 v231, v252, v223
	ds_bpermute_b32 v232, v252, v224
	ds_bpermute_b32 v233, v252, v225
	ds_bpermute_b32 v234, v252, v226
	ds_bpermute_b32 v235, v252, v227
	s_waitcnt lgkmcnt(0)
	v_fma_f32 v248, v220, v232, v224
	v_fma_f32 v249, v221, v233, v225
	v_fma_f32 v250, v222, v234, v226
	v_fma_f32 v251, v223, v235, v227
	v_mul_f32_e32 v228, v220, v228
	v_mul_f32_e32 v229, v221, v229
	v_mul_f32_e32 v230, v222, v230
	v_mul_f32_e32 v231, v223, v231
	v_cndmask_b32_e32 v224, v224, v248, vcc
	v_cndmask_b32_e32 v225, v225, v249, vcc
	v_cndmask_b32_e32 v226, v226, v250, vcc
	v_cndmask_b32_e32 v227, v227, v251, vcc
	v_cndmask_b32_e32 v220, v220, v228, vcc
	v_cndmask_b32_e32 v221, v221, v229, vcc
	v_cndmask_b32_e32 v222, v222, v230, vcc
	v_cndmask_b32_e32 v223, v223, v231, vcc
	v_cmp_le_u32_e32 vcc, 32, v1
	v_add_u32_e32 v252, 0xffffff80, v7
	ds_bpermute_b32 v228, v252, v220
	ds_bpermute_b32 v229, v252, v221
	ds_bpermute_b32 v230, v252, v222
	ds_bpermute_b32 v231, v252, v223
	ds_bpermute_b32 v232, v252, v224
	ds_bpermute_b32 v233, v252, v225
	ds_bpermute_b32 v234, v252, v226
	ds_bpermute_b32 v235, v252, v227
	s_waitcnt lgkmcnt(0)
	v_fma_f32 v248, v220, v232, v224
	v_fma_f32 v249, v221, v233, v225
	v_fma_f32 v250, v222, v234, v226
	v_fma_f32 v251, v223, v235, v227
	v_mul_f32_e32 v228, v220, v228
	v_mul_f32_e32 v229, v221, v229
	v_mul_f32_e32 v230, v222, v230
	v_mul_f32_e32 v231, v223, v231
	v_cndmask_b32_e32 v224, v224, v248, vcc
	v_cndmask_b32_e32 v225, v225, v249, vcc
	v_cndmask_b32_e32 v226, v226, v250, vcc
	v_cndmask_b32_e32 v227, v227, v251, vcc
	v_cndmask_b32_e32 v220, v220, v228, vcc
	v_cndmask_b32_e32 v221, v221, v229, vcc
	v_cndmask_b32_e32 v222, v222, v230, vcc
	v_cndmask_b32_e32 v223, v223, v231, vcc
	v_cmp_lt_u32_e32 vcc, 61, v1
	s_lshl_b32 s13, s12, 6
	v_add_u32_e32 v252, s13, v8
	s_and_saveexec_b64 s[38:39], vcc
	ds_write_b128 v252, v[220:223]
	ds_write_b128 v252, v[224:227] offset:16
	s_or_b64 exec, exec, s[38:39]
	s_waitcnt lgkmcnt(0)
	s_barrier
	v_mov_b32_e32 v244, 0
	v_mov_b32_e32 v245, 0
	v_mov_b32_e32 v246, 0
	v_mov_b32_e32 v247, 0
	ds_read_b128 v[228:231], v8 offset:0
	ds_read_b128 v[232:235], v8 offset:16
	ds_read_b128 v[236:239], v8 offset:64
	ds_read_b128 v[240:243], v8 offset:80
	s_cmp_le_u32 s12, 0
	s_cbranch_scc1 .Lrg_cdone0
	s_waitcnt lgkmcnt(2)
	v_fma_f32 v244, v228, v244, v232
	v_fma_f32 v245, v229, v245, v233
	v_fma_f32 v246, v230, v246, v234
	v_fma_f32 v247, v231, v247, v235
	ds_read_b128 v[228:231], v8 offset:128
	ds_read_b128 v[232:235], v8 offset:144
	s_cmp_le_u32 s12, 1
	s_cbranch_scc1 .Lrg_cdone0
	s_waitcnt lgkmcnt(2)
	v_fma_f32 v244, v236, v244, v240
	v_fma_f32 v245, v237, v245, v241
	v_fma_f32 v246, v238, v246, v242
	v_fma_f32 v247, v239, v247, v243
	ds_read_b128 v[236:239], v8 offset:192
	ds_read_b128 v[240:243], v8 offset:208
	s_cmp_le_u32 s12, 2
	s_cbranch_scc1 .Lrg_cdone0
	s_waitcnt lgkmcnt(2)
	v_fma_f32 v244, v228, v244, v232
	v_fma_f32 v245, v229, v245, v233
	v_fma_f32 v246, v230, v246, v234
	v_fma_f32 v247, v231, v247, v235
	ds_read_b128 v[228:231], v8 offset:256
	ds_read_b128 v[232:235], v8 offset:272
	s_cmp_le_u32 s12, 3
	s_cbranch_scc1 .Lrg_cdone0
	s_waitcnt lgkmcnt(2)
	v_fma_f32 v244, v236, v244, v240
	v_fma_f32 v245, v237, v245, v241
	v_fma_f32 v246, v238, v246, v242
	v_fma_f32 v247, v239, v247, v243
	ds_read_b128 v[236:239], v8 offset:320
	ds_read_b128 v[240:243], v8 offset:336
	s_cmp_le_u32 s12, 4
	s_cbranch_scc1 .Lrg_cdone0
	s_waitcnt lgkmcnt(2)
	v_fma_f32 v244, v228, v244, v232
	v_fma_f32 v245, v229, v245, v233
	v_fma_f32 v246, v230, v246, v234
	v_fma_f32 v247, v231, v247, v235
	ds_read_b128 v[228:231], v8 offset:384
	ds_read_b128 v[232:235], v8 offset:400
	s_cmp_le_u32 s12, 5
	s_cbranch_scc1 .Lrg_cdone0
	s_waitcnt lgkmcnt(2)
	v_fma_f32 v244, v236, v244, v240
	v_fma_f32 v245, v237, v245, v241
	v_fma_f32 v246, v238, v246, v242
	v_fma_f32 v247, v239, v247, v243
	s_cmp_le_u32 s12, 6
	s_cbranch_scc1 .Lrg_cdone0
	s_waitcnt lgkmcnt(0)
	v_fma_f32 v244, v228, v244, v232
	v_fma_f32 v245, v229, v245, v233
	v_fma_f32 v246, v230, v246, v234
	v_fma_f32 v247, v231, v247, v235
